# indexer selection-mask generation: two 128x-unrolled copies replaced by one shared compact block loop (v_writelane ballots, 46 KB less code)
# speedup vs baseline: 1.0022x; 1.0022x over previous
.LBB0_1045:
	s_mov_b32 s27, 0
.Lmg_entry:
	v_cmp_eq_u32_e32 vcc, v4, v23
	v_cmp_ne_u32_e64 s[10:11], 0, v22
	s_and_b64 s[4:5], vcc, s[10:11]
	v_cndmask_b32_e64 v4, 0, 1, s[4:5]
	v_cmp_ne_u32_e32 vcc, 0, v4
	s_cmp_lg_u64 vcc, exec
	s_cselect_b32 s12, 0, 1
	s_mov_b32 s13, 0
	s_cmp_lg_u64 s[20:21], 0
	s_addc_u32 s13, s13, 0
	s_cmp_lg_u64 s[0:1], 0
	s_addc_u32 s13, s13, 0
	s_cmp_lg_u64 s[92:93], 0
	s_addc_u32 s13, s13, 0
	s_cmp_lg_u64 s[6:7], 0
	s_addc_u32 s13, s13, 0
	s_cmp_lg_u64 s[70:71], 0
	s_addc_u32 s13, s13, 0
	s_cmp_lg_u64 s[72:73], 0
	s_addc_u32 s13, s13, 0
	s_cmp_lg_u64 s[56:57], 0
	s_addc_u32 s13, s13, 0
	s_cmp_lg_u64 s[62:63], 0
	s_addc_u32 s13, s13, 0
	v_lshlrev_b32_e64 v0, v76, -1
	v_not_b32_e32 v0, v0
	v_mov_b32_e32 v4, 0
	v_mov_b32_e32 v5, 0
	v_mov_b32_e32 v6, 0
	v_mov_b32_e32 v7, 0
	v_mov_b32_e32 v26, 0
	v_and_b32_e32 v42, 15, v74
	v_lshlrev_b32_e32 v42, 2, v42
	s_mov_b32 s14, 0
.Lmg_blk:
	s_cmp_lg_u32 s14, 4
	s_cbranch_scc1 .Lmg_cp0
	v_mov_b32_e32 v4, v6
	v_mov_b32_e32 v5, v7
	v_mov_b32_e32 v6, 0
	v_mov_b32_e32 v7, 0
.Lmg_cp0:
	s_cmp_lg_u32 s14, 0
	s_cbranch_scc1 .Lmg_cp1
	v_mov_b32_e32 v8, v78
	v_mov_b32_e32 v9, v77
	v_mov_b32_e32 v10, v80
	v_mov_b32_e32 v11, v79
	v_mov_b32_e32 v12, v82
	v_mov_b32_e32 v13, v81
	v_mov_b32_e32 v14, v84
	v_mov_b32_e32 v15, v83
	v_mov_b32_e32 v16, v86
	v_mov_b32_e32 v17, v85
	v_mov_b32_e32 v18, v88
	v_mov_b32_e32 v19, v87
	v_mov_b32_e32 v28, v90
	v_mov_b32_e32 v29, v89
	v_mov_b32_e32 v30, v92
	v_mov_b32_e32 v31, v91
	s_branch .Lmg_body
.Lmg_cp1:
	s_cmp_lg_u32 s14, 1
	s_cbranch_scc1 .Lmg_cp2
	v_mov_b32_e32 v8, v94
	v_mov_b32_e32 v9, v93
	v_mov_b32_e32 v10, v96
	v_mov_b32_e32 v11, v95
	v_mov_b32_e32 v12, v98
	v_mov_b32_e32 v13, v97
	v_mov_b32_e32 v14, v100
	v_mov_b32_e32 v15, v99
	v_mov_b32_e32 v16, v102
	v_mov_b32_e32 v17, v101
	v_mov_b32_e32 v18, v104
	v_mov_b32_e32 v19, v103
	v_mov_b32_e32 v28, v106
	v_mov_b32_e32 v29, v105
	v_mov_b32_e32 v30, v108
	v_mov_b32_e32 v31, v107
	s_branch .Lmg_body
.Lmg_cp2:
	s_cmp_lg_u32 s14, 2
	s_cbranch_scc1 .Lmg_cp3
	v_mov_b32_e32 v8, v110
	v_mov_b32_e32 v9, v109
	v_mov_b32_e32 v10, v112
	v_mov_b32_e32 v11, v111
	v_mov_b32_e32 v12, v114
	v_mov_b32_e32 v13, v113
	v_mov_b32_e32 v14, v116
	v_mov_b32_e32 v15, v115
	v_mov_b32_e32 v16, v118
	v_mov_b32_e32 v17, v117
	v_mov_b32_e32 v18, v120
	v_mov_b32_e32 v19, v119
	v_mov_b32_e32 v28, v122
	v_mov_b32_e32 v29, v121
	v_mov_b32_e32 v30, v124
	v_mov_b32_e32 v31, v123
	s_branch .Lmg_body
.Lmg_cp3:
	s_cmp_lg_u32 s14, 3
	s_cbranch_scc1 .Lmg_cp4
	v_mov_b32_e32 v8, v126
	v_mov_b32_e32 v9, v125
	v_mov_b32_e32 v10, v128
	v_mov_b32_e32 v11, v127
	v_mov_b32_e32 v12, v130
	v_mov_b32_e32 v13, v129
	v_mov_b32_e32 v14, v132
	v_mov_b32_e32 v15, v131
	v_mov_b32_e32 v16, v134
	v_mov_b32_e32 v17, v133
	v_mov_b32_e32 v18, v136
	v_mov_b32_e32 v19, v135
	v_mov_b32_e32 v28, v138
	v_mov_b32_e32 v29, v137
	v_mov_b32_e32 v30, v140
	v_mov_b32_e32 v31, v139
	s_branch .Lmg_body
.Lmg_cp4:
	s_cmp_lg_u32 s14, 4
	s_cbranch_scc1 .Lmg_cp5
	v_mov_b32_e32 v8, v142
	v_mov_b32_e32 v9, v141
	v_mov_b32_e32 v10, v144
	v_mov_b32_e32 v11, v143
	v_mov_b32_e32 v12, v146
	v_mov_b32_e32 v13, v145
	v_mov_b32_e32 v14, v148
	v_mov_b32_e32 v15, v147
	v_mov_b32_e32 v16, v150
	v_mov_b32_e32 v17, v149
	v_mov_b32_e32 v18, v152
	v_mov_b32_e32 v19, v151
	v_mov_b32_e32 v28, v154
	v_mov_b32_e32 v29, v153
	v_mov_b32_e32 v30, v156
	v_mov_b32_e32 v31, v155
	s_branch .Lmg_body
.Lmg_cp5:
	s_cmp_lg_u32 s14, 5
	s_cbranch_scc1 .Lmg_cp6
	v_mov_b32_e32 v8, v158
	v_mov_b32_e32 v9, v157
	v_mov_b32_e32 v10, v160
	v_mov_b32_e32 v11, v159
	v_mov_b32_e32 v12, v162
	v_mov_b32_e32 v13, v161
	v_mov_b32_e32 v14, v164
	v_mov_b32_e32 v15, v163
	v_mov_b32_e32 v16, v166
	v_mov_b32_e32 v17, v165
	v_mov_b32_e32 v18, v168
	v_mov_b32_e32 v19, v167
	v_mov_b32_e32 v28, v170
	v_mov_b32_e32 v29, v169
	v_mov_b32_e32 v30, v172
	v_mov_b32_e32 v31, v171
	s_branch .Lmg_body
.Lmg_cp6:
	s_cmp_lg_u32 s14, 6
	s_cbranch_scc1 .Lmg_cp7
	v_mov_b32_e32 v8, v174
	v_mov_b32_e32 v9, v173
	v_mov_b32_e32 v10, v176
	v_mov_b32_e32 v11, v175
	v_mov_b32_e32 v12, v178
	v_mov_b32_e32 v13, v177
	v_mov_b32_e32 v14, v180
	v_mov_b32_e32 v15, v179
	v_mov_b32_e32 v16, v182
	v_mov_b32_e32 v17, v181
	v_mov_b32_e32 v18, v184
	v_mov_b32_e32 v19, v183
	v_mov_b32_e32 v28, v186
	v_mov_b32_e32 v29, v185
	v_mov_b32_e32 v30, v188
	v_mov_b32_e32 v31, v187
	s_branch .Lmg_body
.Lmg_cp7:
	v_mov_b32_e32 v8, v190
	v_mov_b32_e32 v9, v189
	v_mov_b32_e32 v10, v65
	v_mov_b32_e32 v11, v64
	v_mov_b32_e32 v12, v57
	v_mov_b32_e32 v13, v56
	v_mov_b32_e32 v14, v49
	v_mov_b32_e32 v15, v48
	v_mov_b32_e32 v16, v41
	v_mov_b32_e32 v17, v40
	v_mov_b32_e32 v18, v33
	v_mov_b32_e32 v19, v32
	v_mov_b32_e32 v28, v25
	v_mov_b32_e32 v29, v24
	v_mov_b32_e32 v30, v21
	v_mov_b32_e32 v31, v20
.Lmg_body:
	s_and_b32 s15, s14, 3
	s_lshl_b32 s15, s15, 4
	s_cmp_lg_u32 s12, 0
	s_cbranch_scc1 .Lmg_simple
	s_lshl_b32 s16, s14, 8
	v_or_b32_e32 v27, s16, v76
	v_cmp_eq_u32_e32 vcc, v8, v22
	v_cmp_gt_u32_e64 s[10:11], v8, v22
	v_add_u32_e32 v36, 0, v27
	v_lshrrev_b64 v[34:35], v2, vcc
	v_and_b32_e32 v37, 0xffff, v34
	v_and_b32_e32 v34, v34, v0
	v_bcnt_u32_b32 v34, v34, v26
	v_cmp_lt_i32_e64 s[16:17], v34, v23
	v_cmp_le_i32_e64 s[18:19], v36, v75
	v_bcnt_u32_b32 v26, v37, v26
	s_and_b64 s[4:5], vcc, s[16:17]
	s_or_b64 s[4:5], s[10:11], s[4:5]
	s_and_b64 s[4:5], s[4:5], s[18:19]
	v_writelane_b32 v38, s4, 0
	v_writelane_b32 v39, s5, 0
	v_cmp_eq_u32_e32 vcc, v9, v22
	v_cmp_gt_u32_e64 s[10:11], v9, v22
	v_add_u32_e32 v36, 16, v27
	v_lshrrev_b64 v[34:35], v2, vcc
	v_and_b32_e32 v37, 0xffff, v34
	v_and_b32_e32 v34, v34, v0
	v_bcnt_u32_b32 v34, v34, v26
	v_cmp_lt_i32_e64 s[16:17], v34, v23
	v_cmp_le_i32_e64 s[18:19], v36, v75
	v_bcnt_u32_b32 v26, v37, v26
	s_and_b64 s[4:5], vcc, s[16:17]
	s_or_b64 s[4:5], s[10:11], s[4:5]
	s_and_b64 s[4:5], s[4:5], s[18:19]
	v_writelane_b32 v38, s4, 1
	v_writelane_b32 v39, s5, 1
	v_cmp_eq_u32_e32 vcc, v10, v22
	v_cmp_gt_u32_e64 s[10:11], v10, v22
	v_add_u32_e32 v36, 32, v27
	v_lshrrev_b64 v[34:35], v2, vcc
	v_and_b32_e32 v37, 0xffff, v34
	v_and_b32_e32 v34, v34, v0
	v_bcnt_u32_b32 v34, v34, v26
	v_cmp_lt_i32_e64 s[16:17], v34, v23
	v_cmp_le_i32_e64 s[18:19], v36, v75
	v_bcnt_u32_b32 v26, v37, v26
	s_and_b64 s[4:5], vcc, s[16:17]
	s_or_b64 s[4:5], s[10:11], s[4:5]
	s_and_b64 s[4:5], s[4:5], s[18:19]
	v_writelane_b32 v38, s4, 2
	v_writelane_b32 v39, s5, 2
	v_cmp_eq_u32_e32 vcc, v11, v22
	v_cmp_gt_u32_e64 s[10:11], v11, v22
	v_add_u32_e32 v36, 48, v27
	v_lshrrev_b64 v[34:35], v2, vcc
	v_and_b32_e32 v37, 0xffff, v34
	v_and_b32_e32 v34, v34, v0
	v_bcnt_u32_b32 v34, v34, v26
	v_cmp_lt_i32_e64 s[16:17], v34, v23
	v_cmp_le_i32_e64 s[18:19], v36, v75
	v_bcnt_u32_b32 v26, v37, v26
	s_and_b64 s[4:5], vcc, s[16:17]
	s_or_b64 s[4:5], s[10:11], s[4:5]
	s_and_b64 s[4:5], s[4:5], s[18:19]
	v_writelane_b32 v38, s4, 3
	v_writelane_b32 v39, s5, 3
	v_cmp_eq_u32_e32 vcc, v12, v22
	v_cmp_gt_u32_e64 s[10:11], v12, v22
	v_add_u32_e32 v36, 64, v27
	v_lshrrev_b64 v[34:35], v2, vcc
	v_and_b32_e32 v37, 0xffff, v34
	v_and_b32_e32 v34, v34, v0
	v_bcnt_u32_b32 v34, v34, v26
	v_cmp_lt_i32_e64 s[16:17], v34, v23
	v_cmp_le_i32_e64 s[18:19], v36, v75
	v_bcnt_u32_b32 v26, v37, v26
	s_and_b64 s[4:5], vcc, s[16:17]
	s_or_b64 s[4:5], s[10:11], s[4:5]
	s_and_b64 s[4:5], s[4:5], s[18:19]
	v_writelane_b32 v38, s4, 4
	v_writelane_b32 v39, s5, 4
	v_cmp_eq_u32_e32 vcc, v13, v22
	v_cmp_gt_u32_e64 s[10:11], v13, v22
	v_add_u32_e32 v36, 80, v27
	v_lshrrev_b64 v[34:35], v2, vcc
	v_and_b32_e32 v37, 0xffff, v34
	v_and_b32_e32 v34, v34, v0
	v_bcnt_u32_b32 v34, v34, v26
	v_cmp_lt_i32_e64 s[16:17], v34, v23
	v_cmp_le_i32_e64 s[18:19], v36, v75
	v_bcnt_u32_b32 v26, v37, v26
	s_and_b64 s[4:5], vcc, s[16:17]
	s_or_b64 s[4:5], s[10:11], s[4:5]
	s_and_b64 s[4:5], s[4:5], s[18:19]
	v_writelane_b32 v38, s4, 5
	v_writelane_b32 v39, s5, 5
	v_cmp_eq_u32_e32 vcc, v14, v22
	v_cmp_gt_u32_e64 s[10:11], v14, v22
	v_add_u32_e32 v36, 96, v27
	v_lshrrev_b64 v[34:35], v2, vcc
	v_and_b32_e32 v37, 0xffff, v34
	v_and_b32_e32 v34, v34, v0
	v_bcnt_u32_b32 v34, v34, v26
	v_cmp_lt_i32_e64 s[16:17], v34, v23
	v_cmp_le_i32_e64 s[18:19], v36, v75
	v_bcnt_u32_b32 v26, v37, v26
	s_and_b64 s[4:5], vcc, s[16:17]
	s_or_b64 s[4:5], s[10:11], s[4:5]
	s_and_b64 s[4:5], s[4:5], s[18:19]
	v_writelane_b32 v38, s4, 6
	v_writelane_b32 v39, s5, 6
	v_cmp_eq_u32_e32 vcc, v15, v22
	v_cmp_gt_u32_e64 s[10:11], v15, v22
	v_add_u32_e32 v36, 112, v27
	v_lshrrev_b64 v[34:35], v2, vcc
	v_and_b32_e32 v37, 0xffff, v34
	v_and_b32_e32 v34, v34, v0
	v_bcnt_u32_b32 v34, v34, v26
	v_cmp_lt_i32_e64 s[16:17], v34, v23
	v_cmp_le_i32_e64 s[18:19], v36, v75
	v_bcnt_u32_b32 v26, v37, v26
	s_and_b64 s[4:5], vcc, s[16:17]
	s_or_b64 s[4:5], s[10:11], s[4:5]
	s_and_b64 s[4:5], s[4:5], s[18:19]
	v_writelane_b32 v38, s4, 7
	v_writelane_b32 v39, s5, 7
	v_cmp_eq_u32_e32 vcc, v16, v22
	v_cmp_gt_u32_e64 s[10:11], v16, v22
	v_add_u32_e32 v36, 128, v27
	v_lshrrev_b64 v[34:35], v2, vcc
	v_and_b32_e32 v37, 0xffff, v34
	v_and_b32_e32 v34, v34, v0
	v_bcnt_u32_b32 v34, v34, v26
	v_cmp_lt_i32_e64 s[16:17], v34, v23
	v_cmp_le_i32_e64 s[18:19], v36, v75
	v_bcnt_u32_b32 v26, v37, v26
	s_and_b64 s[4:5], vcc, s[16:17]
	s_or_b64 s[4:5], s[10:11], s[4:5]
	s_and_b64 s[4:5], s[4:5], s[18:19]
	v_writelane_b32 v38, s4, 8
	v_writelane_b32 v39, s5, 8
	v_cmp_eq_u32_e32 vcc, v17, v22
	v_cmp_gt_u32_e64 s[10:11], v17, v22
	v_add_u32_e32 v36, 144, v27
	v_lshrrev_b64 v[34:35], v2, vcc
	v_and_b32_e32 v37, 0xffff, v34
	v_and_b32_e32 v34, v34, v0
	v_bcnt_u32_b32 v34, v34, v26
	v_cmp_lt_i32_e64 s[16:17], v34, v23
	v_cmp_le_i32_e64 s[18:19], v36, v75
	v_bcnt_u32_b32 v26, v37, v26
	s_and_b64 s[4:5], vcc, s[16:17]
	s_or_b64 s[4:5], s[10:11], s[4:5]
	s_and_b64 s[4:5], s[4:5], s[18:19]
	v_writelane_b32 v38, s4, 9
	v_writelane_b32 v39, s5, 9
	v_cmp_eq_u32_e32 vcc, v18, v22
	v_cmp_gt_u32_e64 s[10:11], v18, v22
	v_add_u32_e32 v36, 160, v27
	v_lshrrev_b64 v[34:35], v2, vcc
	v_and_b32_e32 v37, 0xffff, v34
	v_and_b32_e32 v34, v34, v0
	v_bcnt_u32_b32 v34, v34, v26
	v_cmp_lt_i32_e64 s[16:17], v34, v23
	v_cmp_le_i32_e64 s[18:19], v36, v75
	v_bcnt_u32_b32 v26, v37, v26
	s_and_b64 s[4:5], vcc, s[16:17]
	s_or_b64 s[4:5], s[10:11], s[4:5]
	s_and_b64 s[4:5], s[4:5], s[18:19]
	v_writelane_b32 v38, s4, 10
	v_writelane_b32 v39, s5, 10
	v_cmp_eq_u32_e32 vcc, v19, v22
	v_cmp_gt_u32_e64 s[10:11], v19, v22
	v_add_u32_e32 v36, 176, v27
	v_lshrrev_b64 v[34:35], v2, vcc
	v_and_b32_e32 v37, 0xffff, v34
	v_and_b32_e32 v34, v34, v0
	v_bcnt_u32_b32 v34, v34, v26
	v_cmp_lt_i32_e64 s[16:17], v34, v23
	v_cmp_le_i32_e64 s[18:19], v36, v75
	v_bcnt_u32_b32 v26, v37, v26
	s_and_b64 s[4:5], vcc, s[16:17]
	s_or_b64 s[4:5], s[10:11], s[4:5]
	s_and_b64 s[4:5], s[4:5], s[18:19]
	v_writelane_b32 v38, s4, 11
	v_writelane_b32 v39, s5, 11
	v_cmp_eq_u32_e32 vcc, v28, v22
	v_cmp_gt_u32_e64 s[10:11], v28, v22
	v_add_u32_e32 v36, 192, v27
	v_lshrrev_b64 v[34:35], v2, vcc
	v_and_b32_e32 v37, 0xffff, v34
	v_and_b32_e32 v34, v34, v0
	v_bcnt_u32_b32 v34, v34, v26
	v_cmp_lt_i32_e64 s[16:17], v34, v23
	v_cmp_le_i32_e64 s[18:19], v36, v75
	v_bcnt_u32_b32 v26, v37, v26
	s_and_b64 s[4:5], vcc, s[16:17]
	s_or_b64 s[4:5], s[10:11], s[4:5]
	s_and_b64 s[4:5], s[4:5], s[18:19]
	v_writelane_b32 v38, s4, 12
	v_writelane_b32 v39, s5, 12
	v_cmp_eq_u32_e32 vcc, v29, v22
	v_cmp_gt_u32_e64 s[10:11], v29, v22
	v_add_u32_e32 v36, 208, v27
	v_lshrrev_b64 v[34:35], v2, vcc
	v_and_b32_e32 v37, 0xffff, v34
	v_and_b32_e32 v34, v34, v0
	v_bcnt_u32_b32 v34, v34, v26
	v_cmp_lt_i32_e64 s[16:17], v34, v23
	v_cmp_le_i32_e64 s[18:19], v36, v75
	v_bcnt_u32_b32 v26, v37, v26
	s_and_b64 s[4:5], vcc, s[16:17]
	s_or_b64 s[4:5], s[10:11], s[4:5]
	s_and_b64 s[4:5], s[4:5], s[18:19]
	v_writelane_b32 v38, s4, 13
	v_writelane_b32 v39, s5, 13
	v_cmp_eq_u32_e32 vcc, v30, v22
	v_cmp_gt_u32_e64 s[10:11], v30, v22
	v_add_u32_e32 v36, 224, v27
	v_lshrrev_b64 v[34:35], v2, vcc
	v_and_b32_e32 v37, 0xffff, v34
	v_and_b32_e32 v34, v34, v0
	v_bcnt_u32_b32 v34, v34, v26
	v_cmp_lt_i32_e64 s[16:17], v34, v23
	v_cmp_le_i32_e64 s[18:19], v36, v75
	v_bcnt_u32_b32 v26, v37, v26
	s_and_b64 s[4:5], vcc, s[16:17]
	s_or_b64 s[4:5], s[10:11], s[4:5]
	s_and_b64 s[4:5], s[4:5], s[18:19]
	v_writelane_b32 v38, s4, 14
	v_writelane_b32 v39, s5, 14
	v_cmp_eq_u32_e32 vcc, v31, v22
	v_cmp_gt_u32_e64 s[10:11], v31, v22
	v_add_u32_e32 v36, 240, v27
	v_lshrrev_b64 v[34:35], v2, vcc
	v_and_b32_e32 v37, 0xffff, v34
	v_and_b32_e32 v34, v34, v0
	v_bcnt_u32_b32 v34, v34, v26
	v_cmp_lt_i32_e64 s[16:17], v34, v23
	v_cmp_le_i32_e64 s[18:19], v36, v75
	v_bcnt_u32_b32 v26, v37, v26
	s_and_b64 s[4:5], vcc, s[16:17]
	s_or_b64 s[4:5], s[10:11], s[4:5]
	s_and_b64 s[4:5], s[4:5], s[18:19]
	v_writelane_b32 v38, s4, 15
	v_writelane_b32 v39, s5, 15
	s_branch .Lmg_next
.Lmg_simple:
	v_cmp_ge_u32_e64 s[16:17], v8, v22
	v_cmp_ge_u32_e64 s[18:19], v9, v22
	v_cmp_ge_u32_e64 s[22:23], v10, v22
	v_cmp_ge_u32_e64 s[24:25], v11, v22
	v_cmp_ge_u32_e64 s[28:29], v12, v22
	v_cmp_ge_u32_e64 s[30:31], v13, v22
	v_cmp_ge_u32_e64 s[32:33], v14, v22
	v_cmp_ge_u32_e64 s[34:35], v15, v22
	v_writelane_b32 v38, s16, 0
	v_writelane_b32 v39, s17, 0
	v_writelane_b32 v38, s18, 1
	v_writelane_b32 v39, s19, 1
	v_writelane_b32 v38, s22, 2
	v_writelane_b32 v39, s23, 2
	v_writelane_b32 v38, s24, 3
	v_writelane_b32 v39, s25, 3
	v_writelane_b32 v38, s28, 4
	v_writelane_b32 v39, s29, 4
	v_writelane_b32 v38, s30, 5
	v_writelane_b32 v39, s31, 5
	v_writelane_b32 v38, s32, 6
	v_writelane_b32 v39, s33, 6
	v_writelane_b32 v38, s34, 7
	v_writelane_b32 v39, s35, 7
	v_cmp_ge_u32_e64 s[16:17], v16, v22
	v_cmp_ge_u32_e64 s[18:19], v17, v22
	v_cmp_ge_u32_e64 s[22:23], v18, v22
	v_cmp_ge_u32_e64 s[24:25], v19, v22
	v_cmp_ge_u32_e64 s[28:29], v28, v22
	v_cmp_ge_u32_e64 s[30:31], v29, v22
	v_cmp_ge_u32_e64 s[32:33], v30, v22
	v_cmp_ge_u32_e64 s[34:35], v31, v22
	v_writelane_b32 v38, s16, 8
	v_writelane_b32 v39, s17, 8
	v_writelane_b32 v38, s18, 9
	v_writelane_b32 v39, s19, 9
	v_writelane_b32 v38, s22, 10
	v_writelane_b32 v39, s23, 10
	v_writelane_b32 v38, s24, 11
	v_writelane_b32 v39, s25, 11
	v_writelane_b32 v38, s28, 12
	v_writelane_b32 v39, s29, 12
	v_writelane_b32 v38, s30, 13
	v_writelane_b32 v39, s31, 13
	v_writelane_b32 v38, s32, 14
	v_writelane_b32 v39, s33, 14
	v_writelane_b32 v38, s34, 15
	v_writelane_b32 v39, s35, 15
.Lmg_next:
	ds_bpermute_b32 v34, v42, v38
	ds_bpermute_b32 v35, v42, v39
	s_mov_b32 s16, 0xffff
	s_mov_b32 s17, 0
	s_lshl_b64 s[16:17], s[16:17], s15
	s_waitcnt lgkmcnt(0)
	v_cndmask_b32_e64 v6, v6, v34, s[16:17]
	v_cndmask_b32_e64 v7, v7, v35, s[16:17]
	s_add_i32 s14, s14, 1
	s_cmp_lt_u32 s14, s13
	s_cbranch_scc1 .Lmg_blk
	s_cmp_gt_u32 s13, 4
	s_cbranch_scc1 .Lmg_done
	v_mov_b32_e32 v4, v6
	v_mov_b32_e32 v5, v7
	v_mov_b32_e32 v6, 0
	v_mov_b32_e32 v7, 0
.Lmg_done:
	s_cmp_lg_u32 s27, 0
	s_cbranch_scc1 .LBB0_1434
	s_branch .LBB0_611

.LBB0_1402:
	s_mov_b32 s27, 1
	s_branch .Lmg_entry
.LBB0_1434:
	s_ashr_i32 s0, s81, 2
	s_ashr_i32 s1, s0, 31
	s_lshl_b64 s[0:1], s[0:1], 10
	s_add_u32 s0, s89, s0
	s_addc_u32 s1, s94, s1
	v_lshlrev_b32_e32 v2, 3, v74
	global_store_dwordx2 v2, v[4:5], s[0:1]
	global_store_dwordx2 v2, v[6:7], s[0:1] offset:512
	s_mov_b32 s81, s44
	s_mov_b32 s44, s45
	s_mov_b32 s45, s91
	v_readlane_b32 s91, v255, 52
	s_cbranch_execz .LBB0_663
	s_branch .LBB0_668
.LBB0_1439:
	v_readlane_b32 s65, v255, 19
	v_readlane_b32 s94, v254, 57
	s_add_i32 s33, s65, 2
	v_readlane_b32 s95, v254, 58
	s_cmp_ge_i32 s33, s95
	s_cbranch_scc1 .LBB0_1452
	s_waitcnt vmcnt(0)
	s_barrier
	s_mov_b64 s[0:1], exec
	v_readlane_b32 s4, v254, 5
	v_readlane_b32 s5, v254, 6
	v_readlane_b32 s92, v254, 55
	v_readlane_b32 s68, v255, 17
	s_and_b64 s[4:5], s[0:1], s[4:5]
	v_readlane_b32 s93, v254, 56
	v_readlane_b32 s96, v254, 59
	v_readlane_b32 s91, v255, 21
	v_readlane_b32 s76, v255, 22
	v_readlane_b32 s69, v255, 18
	v_readlane_b32 s45, v255, 20
	s_mov_b64 exec, s[4:5]
	s_cbranch_execz .LBB0_1485
	v_readlane_b32 s4, v254, 2
	v_readlane_b32 s6, v254, 39
	v_readlane_b32 s5, v254, 3
	v_readlane_b32 s42, v254, 4
	v_mov_b32_e32 v2, s6
	s_waitcnt vmcnt(0) expcnt(0) lgkmcnt(0)
	ds_read_b32 v4, v2
	v_readlane_b32 s6, v254, 40
	s_waitcnt lgkmcnt(0)
	v_cmp_ne_u32_e32 vcc, 0, v4
	v_mov_b32_e32 v2, s6
	ds_read_b32 v2, v2
	s_cbranch_vccnz .LBB0_1456
	v_readlane_b32 s6, v254, 0
	v_readlane_b32 s7, v254, 1
	s_load_dwordx2 s[12:13], s[6:7], 0x4
	s_add_u32 s6, s4, 0x1000
	s_addc_u32 s7, s5, 0
	s_add_u32 s10, s4, 0x1100
	s_addc_u32 s11, s5, 0
	s_waitcnt lgkmcnt(0)
	s_mul_i32 s36, s12, s3
	s_add_u32 s12, s4, 0x1200
	s_mul_i32 s36, s36, s13
	s_addc_u32 s13, s5, 0
	s_add_u32 s14, s4, 0x1300
	s_addc_u32 s15, s5, 0
	s_mov_b32 s37, 1
	s_mov_b64 s[16:17], 0
	s_branch .LBB0_1445
